# MoE fifth-round half units also skip the A-operand LDS fragment reads of the row half they do not compute
# speedup vs baseline: 1.0041x; 1.0041x over previous
.Lt9_flag:
.LBB0_1392:
	s_add_u32 s24, s74, s22
	s_addc_u32 s25, s75, s23
	s_add_u32 s26, s24, 0xd851100
	s_addc_u32 s27, s25, 0
	s_add_u32 s45, s42, s22
	s_addc_u32 s46, s43, s23
	s_add_i32 s47, 0, 0x10000
	s_cmpk_eq_i32 s22, 0x700
	s_cselect_b64 vcc, -1, 0
	s_and_b64 s[24:25], vcc, exec
	s_cselect_b32 s27, s59, s27
	s_cselect_b32 s26, s58, s26
	v_add_u32_e32 v161, s47, v154
	s_cselect_b32 s25, s17, s46
	s_cselect_b32 s24, s41, s45
	s_add_i32 s45, 0, 0x14000
	ds_read_b128 v[162:165], v161
	ds_read_b128 v[166:169], v161 offset:1024
	ds_read_b128 v[170:173], v161 offset:2048
	ds_read_b128 v[174:177], v161 offset:3072
	v_add_u32_e32 v161, s45, v154
	ds_read_b128 v[178:181], v161
	ds_read_b128 v[182:185], v161 offset:1024
	ds_read_b128 v[186:189], v161 offset:2048
	ds_read_b128 v[190:193], v161 offset:3072
	v_cndmask_b32_e32 v114, v138, v158, vcc
	v_cndmask_b32_e32 v137, v136, v160, vcc
	v_cndmask_b32_e32 v222, v142, v157, vcc
	v_cndmask_b32_e32 v141, v140, v159, vcc
	v_lshl_add_u64 v[238:239], v[146:147], 0, s[22:23]
	s_add_i32 m0, s21, 0xc000
	s_bitcmp1_b32 s36, 0
	s_cbranch_scc1 .Lt9_r0
	ds_read_b128 v[194:197], v143
	ds_read_b128 v[198:201], v143 offset:1024
	ds_read_b128 v[202:205], v143 offset:2048
	ds_read_b128 v[206:209], v143 offset:3072
	ds_read_b128 v[210:213], v143 offset:4096
	ds_read_b128 v[214:217], v143 offset:5120
	ds_read_b128 v[218:221], v143 offset:6144
	ds_read_b128 v[234:237], v143 offset:7168
.Lt9_r0:
	global_load_lds_dwordx4 v[238:239], off
	v_lshl_add_u64 v[238:239], v[144:145], 0, s[22:23]
	s_add_i32 m0, s21, 0xe000
	s_nop 0
	global_load_lds_dwordx4 v[238:239], off
	s_waitcnt vmcnt(8)
	s_waitcnt lgkmcnt(0)
	s_barrier
	s_bitcmp1_b32 s36, 0
	s_cbranch_scc1 .Lt9_k0
	s_setprio 1
	s_waitcnt lgkmcnt(0)
	v_mfma_f32_16x16x32_bf16 v[128:131], v[162:165], v[194:197], v[128:131]
	v_mfma_f32_16x16x32_bf16 v[124:127], v[170:173], v[194:197], v[124:127]
	v_mfma_f32_16x16x32_bf16 v[110:113], v[162:165], v[202:205], v[110:113]
	v_mfma_f32_16x16x32_bf16 v[106:109], v[170:173], v[202:205], v[106:109]
	v_mfma_f32_16x16x32_bf16 v[94:97], v[162:165], v[210:213], v[94:97]
	v_mfma_f32_16x16x32_bf16 v[90:93], v[170:173], v[210:213], v[90:93]
	v_mfma_f32_16x16x32_bf16 v[78:81], v[162:165], v[218:221], v[78:81]
	v_mfma_f32_16x16x32_bf16 v[74:77], v[170:173], v[218:221], v[74:77]
	v_mfma_f32_16x16x32_bf16 v[128:131], v[166:169], v[198:201], v[128:131]
	v_mfma_f32_16x16x32_bf16 v[124:127], v[174:177], v[198:201], v[124:127]
	v_mfma_f32_16x16x32_bf16 v[110:113], v[166:169], v[206:209], v[110:113]
	v_mfma_f32_16x16x32_bf16 v[106:109], v[174:177], v[206:209], v[106:109]
	v_mfma_f32_16x16x32_bf16 v[94:97], v[166:169], v[214:217], v[94:97]
	v_mfma_f32_16x16x32_bf16 v[90:93], v[174:177], v[214:217], v[90:93]
	v_mfma_f32_16x16x32_bf16 v[78:81], v[166:169], v[234:237], v[78:81]
	v_mfma_f32_16x16x32_bf16 v[74:77], v[174:177], v[234:237], v[74:77]
	s_setprio 0
	s_setprio 1
	v_mfma_f32_16x16x32_bf16 v[120:123], v[178:181], v[194:197], v[120:123]
	v_mfma_f32_16x16x32_bf16 v[116:119], v[186:189], v[194:197], v[116:119]
	v_mfma_f32_16x16x32_bf16 v[102:105], v[178:181], v[202:205], v[102:105]
	v_mfma_f32_16x16x32_bf16 v[98:101], v[186:189], v[202:205], v[98:101]
	v_mfma_f32_16x16x32_bf16 v[86:89], v[178:181], v[210:213], v[86:89]
	v_mfma_f32_16x16x32_bf16 v[82:85], v[186:189], v[210:213], v[82:85]
	v_mfma_f32_16x16x32_bf16 v[70:73], v[178:181], v[218:221], v[70:73]
	v_mfma_f32_16x16x32_bf16 v[66:69], v[186:189], v[218:221], v[66:69]
	v_mfma_f32_16x16x32_bf16 v[120:123], v[182:185], v[198:201], v[120:123]
	v_mfma_f32_16x16x32_bf16 v[116:119], v[190:193], v[198:201], v[116:119]
	v_mfma_f32_16x16x32_bf16 v[102:105], v[182:185], v[206:209], v[102:105]
	v_mfma_f32_16x16x32_bf16 v[98:101], v[190:193], v[206:209], v[98:101]
	v_mfma_f32_16x16x32_bf16 v[86:89], v[182:185], v[214:217], v[86:89]
	v_mfma_f32_16x16x32_bf16 v[82:85], v[190:193], v[214:217], v[82:85]
	v_mfma_f32_16x16x32_bf16 v[70:73], v[182:185], v[234:237], v[70:73]
	v_mfma_f32_16x16x32_bf16 v[66:69], v[190:193], v[234:237], v[66:69]
	s_setprio 0
.Lt9_k0:
	s_barrier
	s_add_i32 s46, s47, s2
	v_lshl_add_u64 v[238:239], s[24:25], 0, v[132:133]
	s_mov_b32 m0, s46
	s_bitcmp1_b32 s36, 1
	s_cbranch_scc1 .Lt9_r1
	ds_read_b128 v[194:197], v143 offset:16384
	ds_read_b128 v[198:201], v143 offset:17408
	ds_read_b128 v[202:205], v143 offset:18432
	ds_read_b128 v[206:209], v143 offset:19456
	ds_read_b128 v[210:213], v143 offset:20480
	ds_read_b128 v[214:217], v143 offset:21504
	ds_read_b128 v[218:221], v143 offset:22528
	ds_read_b128 v[234:237], v143 offset:23552
.Lt9_r1:
	global_load_lds_dwordx4 v[238:239], off
	s_add_i32 m0, s46, 0x2000
	s_add_u32 s46, s24, 0x40000
	v_lshl_add_u64 v[240:241], s[24:25], 0, v[134:135]
	s_addc_u32 s47, s25, 0
	s_add_i32 s45, s45, s2
	global_load_lds_dwordx4 v[240:241], off
	v_lshl_add_u64 v[242:243], s[46:47], 0, v[132:133]
	s_mov_b32 m0, s45
	v_mov_b32_e32 v223, v115
	global_load_lds_dwordx4 v[242:243], off
	v_lshl_add_u64 v[242:243], s[46:47], 0, v[134:135]
	s_add_i32 m0, s45, 0x2000
	s_nop 0
	global_load_lds_dwordx4 v[242:243], off
	s_mov_b32 m0, s21
	v_lshl_add_u64 v[242:243], s[26:27], 0, v[114:115]
	global_load_lds_dwordx4 v114, s[26:27]
	s_mov_b32 m0, s29
	s_nop 0
	global_load_lds_dwordx4 v222, s[26:27]
	s_waitcnt vmcnt(8)
	s_waitcnt lgkmcnt(0)
	v_lshl_add_u64 v[222:223], s[26:27], 0, v[222:223]
	s_barrier
	s_bitcmp1_b32 s36, 1
	s_cbranch_scc1 .Lt9_k1
	s_setprio 1
	s_waitcnt lgkmcnt(0)
	v_mfma_f32_16x16x32_bf16 v[62:65], v[162:165], v[194:197], v[62:65]
	v_mfma_f32_16x16x32_bf16 v[58:61], v[170:173], v[194:197], v[58:61]
	v_mfma_f32_16x16x32_bf16 v[46:49], v[162:165], v[202:205], v[46:49]
	v_mfma_f32_16x16x32_bf16 v[42:45], v[170:173], v[202:205], v[42:45]
	v_mfma_f32_16x16x32_bf16 v[30:33], v[162:165], v[210:213], v[30:33]
	v_mfma_f32_16x16x32_bf16 v[26:29], v[170:173], v[210:213], v[26:29]
	v_mfma_f32_16x16x32_bf16 v[14:17], v[162:165], v[218:221], v[14:17]
	v_mfma_f32_16x16x32_bf16 v[10:13], v[170:173], v[218:221], v[10:13]
	v_mfma_f32_16x16x32_bf16 v[62:65], v[166:169], v[198:201], v[62:65]
	v_mfma_f32_16x16x32_bf16 v[58:61], v[174:177], v[198:201], v[58:61]
	v_mfma_f32_16x16x32_bf16 v[46:49], v[166:169], v[206:209], v[46:49]
	v_mfma_f32_16x16x32_bf16 v[42:45], v[174:177], v[206:209], v[42:45]
	v_mfma_f32_16x16x32_bf16 v[30:33], v[166:169], v[214:217], v[30:33]
	v_mfma_f32_16x16x32_bf16 v[26:29], v[174:177], v[214:217], v[26:29]
	v_mfma_f32_16x16x32_bf16 v[14:17], v[166:169], v[234:237], v[14:17]
	v_mfma_f32_16x16x32_bf16 v[10:13], v[174:177], v[234:237], v[10:13]
	s_setprio 0
	s_setprio 1
	v_mfma_f32_16x16x32_bf16 v[54:57], v[178:181], v[194:197], v[54:57]
	v_mfma_f32_16x16x32_bf16 v[50:53], v[186:189], v[194:197], v[50:53]
	v_mfma_f32_16x16x32_bf16 v[38:41], v[178:181], v[202:205], v[38:41]
	v_mfma_f32_16x16x32_bf16 v[34:37], v[186:189], v[202:205], v[34:37]
	v_mfma_f32_16x16x32_bf16 v[22:25], v[178:181], v[210:213], v[22:25]
	v_mfma_f32_16x16x32_bf16 v[18:21], v[186:189], v[210:213], v[18:21]
	v_mfma_f32_16x16x32_bf16 v[6:9], v[178:181], v[218:221], v[6:9]
	v_mfma_f32_16x16x32_bf16 v[2:5], v[186:189], v[218:221], v[2:5]
	v_mfma_f32_16x16x32_bf16 v[54:57], v[182:185], v[198:201], v[54:57]
	v_mfma_f32_16x16x32_bf16 v[50:53], v[190:193], v[198:201], v[50:53]
	v_mfma_f32_16x16x32_bf16 v[38:41], v[182:185], v[206:209], v[38:41]
	v_mfma_f32_16x16x32_bf16 v[34:37], v[190:193], v[206:209], v[34:37]
	v_mfma_f32_16x16x32_bf16 v[22:25], v[182:185], v[214:217], v[22:25]
	v_mfma_f32_16x16x32_bf16 v[18:21], v[190:193], v[214:217], v[18:21]
	v_mfma_f32_16x16x32_bf16 v[6:9], v[182:185], v[234:237], v[6:9]
	v_mfma_f32_16x16x32_bf16 v[2:5], v[190:193], v[234:237], v[2:5]
	s_setprio 0
.Lt9_k1:
	s_barrier
	s_add_i32 s45, 0, 0x18000
	v_add_u32_e32 v114, s45, v154
	s_add_i32 s46, 0, 0x1c000
	ds_read_b128 v[162:165], v114
	ds_read_b128 v[166:169], v114 offset:1024
	ds_read_b128 v[170:173], v114 offset:2048
	ds_read_b128 v[174:177], v114 offset:3072
	v_add_u32_e32 v114, s46, v154
	ds_read_b128 v[178:181], v114
	ds_read_b128 v[182:185], v114 offset:1024
	ds_read_b128 v[186:189], v114 offset:2048
	ds_read_b128 v[190:193], v114 offset:3072
	s_mov_b32 m0, s30
	s_bitcmp1_b32 s36, 0
	s_cbranch_scc1 .Lt9_r2
	ds_read_b128 v[194:197], v143 offset:32768
	ds_read_b128 v[198:201], v143 offset:33792
	ds_read_b128 v[202:205], v143 offset:34816
	ds_read_b128 v[206:209], v143 offset:35840
	ds_read_b128 v[210:213], v143 offset:36864
	ds_read_b128 v[214:217], v143 offset:37888
	ds_read_b128 v[218:221], v143 offset:38912
	ds_read_b128 v[234:237], v143 offset:39936
.Lt9_r2:
	global_load_lds_dwordx4 v137, s[26:27]
	s_mov_b32 m0, s31
	s_nop 0
	global_load_lds_dwordx4 v141, s[26:27]
	s_waitcnt vmcnt(8)
	s_waitcnt lgkmcnt(0)
	s_barrier
	s_bitcmp1_b32 s36, 0
	s_cbranch_scc1 .Lt9_k2
	s_setprio 1
	s_waitcnt lgkmcnt(0)
	v_mfma_f32_16x16x32_bf16 v[128:131], v[162:165], v[194:197], v[128:131]
	v_mfma_f32_16x16x32_bf16 v[124:127], v[170:173], v[194:197], v[124:127]
	v_mfma_f32_16x16x32_bf16 v[110:113], v[162:165], v[202:205], v[110:113]
	v_mfma_f32_16x16x32_bf16 v[106:109], v[170:173], v[202:205], v[106:109]
	v_mfma_f32_16x16x32_bf16 v[94:97], v[162:165], v[210:213], v[94:97]
	v_mfma_f32_16x16x32_bf16 v[90:93], v[170:173], v[210:213], v[90:93]
	v_mfma_f32_16x16x32_bf16 v[78:81], v[162:165], v[218:221], v[78:81]
	v_mfma_f32_16x16x32_bf16 v[74:77], v[170:173], v[218:221], v[74:77]
	v_mfma_f32_16x16x32_bf16 v[128:131], v[166:169], v[198:201], v[128:131]
	v_mfma_f32_16x16x32_bf16 v[124:127], v[174:177], v[198:201], v[124:127]
	v_mfma_f32_16x16x32_bf16 v[110:113], v[166:169], v[206:209], v[110:113]
	v_mfma_f32_16x16x32_bf16 v[106:109], v[174:177], v[206:209], v[106:109]
	v_mfma_f32_16x16x32_bf16 v[94:97], v[166:169], v[214:217], v[94:97]
	v_mfma_f32_16x16x32_bf16 v[90:93], v[174:177], v[214:217], v[90:93]
	v_mfma_f32_16x16x32_bf16 v[78:81], v[166:169], v[234:237], v[78:81]
	v_mfma_f32_16x16x32_bf16 v[74:77], v[174:177], v[234:237], v[74:77]
	s_setprio 0
	s_setprio 1
	v_mfma_f32_16x16x32_bf16 v[120:123], v[178:181], v[194:197], v[120:123]
	v_mfma_f32_16x16x32_bf16 v[116:119], v[186:189], v[194:197], v[116:119]
	v_mfma_f32_16x16x32_bf16 v[102:105], v[178:181], v[202:205], v[102:105]
	v_mfma_f32_16x16x32_bf16 v[98:101], v[186:189], v[202:205], v[98:101]
	v_mfma_f32_16x16x32_bf16 v[86:89], v[178:181], v[210:213], v[86:89]
	v_mfma_f32_16x16x32_bf16 v[82:85], v[186:189], v[210:213], v[82:85]
	v_mfma_f32_16x16x32_bf16 v[70:73], v[178:181], v[218:221], v[70:73]
	v_mfma_f32_16x16x32_bf16 v[66:69], v[186:189], v[218:221], v[66:69]
	v_mfma_f32_16x16x32_bf16 v[120:123], v[182:185], v[198:201], v[120:123]
	v_mfma_f32_16x16x32_bf16 v[116:119], v[190:193], v[198:201], v[116:119]
	v_mfma_f32_16x16x32_bf16 v[102:105], v[182:185], v[206:209], v[102:105]
	v_mfma_f32_16x16x32_bf16 v[98:101], v[190:193], v[206:209], v[98:101]
	v_mfma_f32_16x16x32_bf16 v[86:89], v[182:185], v[214:217], v[86:89]
	v_mfma_f32_16x16x32_bf16 v[82:85], v[190:193], v[214:217], v[82:85]
	v_mfma_f32_16x16x32_bf16 v[70:73], v[182:185], v[234:237], v[70:73]
	v_mfma_f32_16x16x32_bf16 v[66:69], v[190:193], v[234:237], v[66:69]
	s_setprio 0
.Lt9_k2:
	s_barrier
	s_add_i32 s26, s45, s2
	v_lshl_add_u64 v[238:239], v[238:239], 0, s[78:79]
	s_mov_b32 m0, s26
	s_bitcmp1_b32 s36, 1
	s_cbranch_scc1 .Lt9_r3
	ds_read_b128 v[194:197], v143 offset:49152
	ds_read_b128 v[198:201], v143 offset:50176
	ds_read_b128 v[202:205], v143 offset:51200
	ds_read_b128 v[206:209], v143 offset:52224
	ds_read_b128 v[210:213], v143 offset:53248
	ds_read_b128 v[214:217], v143 offset:54272
	ds_read_b128 v[218:221], v143 offset:55296
	ds_read_b128 v[234:237], v143 offset:56320
.Lt9_r3:
	global_load_lds_dwordx4 v[238:239], off
	s_add_i32 m0, s26, 0x2000
	s_add_u32 s24, s24, 0x40080
	v_lshl_add_u64 v[238:239], v[240:241], 0, s[78:79]
	s_addc_u32 s25, s25, 0
	s_add_i32 s26, s46, s2
	global_load_lds_dwordx4 v[238:239], off
	v_lshl_add_u64 v[238:239], s[24:25], 0, v[132:133]
	s_mov_b32 m0, s26
	v_lshl_add_u64 v[222:223], v[222:223], 0, s[78:79]
	global_load_lds_dwordx4 v[238:239], off
	v_lshl_add_u64 v[238:239], s[24:25], 0, v[134:135]
	s_add_i32 m0, s26, 0x2000
	s_nop 0
	global_load_lds_dwordx4 v[238:239], off
	v_lshl_add_u64 v[238:239], v[242:243], 0, s[78:79]
	s_mov_b32 m0, s34
	s_nop 0
	global_load_lds_dwordx4 v[238:239], off
	s_mov_b32 m0, s35
	s_nop 0
	global_load_lds_dwordx4 v[222:223], off
	s_waitcnt vmcnt(8)
	s_waitcnt lgkmcnt(0)
	s_barrier
	s_bitcmp1_b32 s36, 1
	s_cbranch_scc1 .Lt9_k3
	s_setprio 1
	s_waitcnt lgkmcnt(0)
	v_mfma_f32_16x16x32_bf16 v[62:65], v[162:165], v[194:197], v[62:65]
	v_mfma_f32_16x16x32_bf16 v[58:61], v[170:173], v[194:197], v[58:61]
	v_mfma_f32_16x16x32_bf16 v[46:49], v[162:165], v[202:205], v[46:49]
	v_mfma_f32_16x16x32_bf16 v[42:45], v[170:173], v[202:205], v[42:45]
	v_mfma_f32_16x16x32_bf16 v[30:33], v[162:165], v[210:213], v[30:33]
	v_mfma_f32_16x16x32_bf16 v[26:29], v[170:173], v[210:213], v[26:29]
	v_mfma_f32_16x16x32_bf16 v[14:17], v[162:165], v[218:221], v[14:17]
	v_mfma_f32_16x16x32_bf16 v[10:13], v[170:173], v[218:221], v[10:13]
	v_mfma_f32_16x16x32_bf16 v[62:65], v[166:169], v[198:201], v[62:65]
	v_mfma_f32_16x16x32_bf16 v[58:61], v[174:177], v[198:201], v[58:61]
	v_mfma_f32_16x16x32_bf16 v[46:49], v[166:169], v[206:209], v[46:49]
	v_mfma_f32_16x16x32_bf16 v[42:45], v[174:177], v[206:209], v[42:45]
	v_mfma_f32_16x16x32_bf16 v[30:33], v[166:169], v[214:217], v[30:33]
	v_mfma_f32_16x16x32_bf16 v[26:29], v[174:177], v[214:217], v[26:29]
	v_mfma_f32_16x16x32_bf16 v[14:17], v[166:169], v[234:237], v[14:17]
	v_mfma_f32_16x16x32_bf16 v[10:13], v[174:177], v[234:237], v[10:13]
	s_setprio 0
	s_setprio 1
	v_mfma_f32_16x16x32_bf16 v[54:57], v[178:181], v[194:197], v[54:57]
	v_mfma_f32_16x16x32_bf16 v[50:53], v[186:189], v[194:197], v[50:53]
	v_mfma_f32_16x16x32_bf16 v[38:41], v[178:181], v[202:205], v[38:41]
	v_mfma_f32_16x16x32_bf16 v[34:37], v[186:189], v[202:205], v[34:37]
	v_mfma_f32_16x16x32_bf16 v[22:25], v[178:181], v[210:213], v[22:25]
	v_mfma_f32_16x16x32_bf16 v[18:21], v[186:189], v[210:213], v[18:21]
	v_mfma_f32_16x16x32_bf16 v[6:9], v[178:181], v[218:221], v[6:9]
	v_mfma_f32_16x16x32_bf16 v[2:5], v[186:189], v[218:221], v[2:5]
	v_mfma_f32_16x16x32_bf16 v[54:57], v[182:185], v[198:201], v[54:57]
	v_mfma_f32_16x16x32_bf16 v[50:53], v[190:193], v[198:201], v[50:53]
	v_mfma_f32_16x16x32_bf16 v[38:41], v[182:185], v[206:209], v[38:41]
	v_mfma_f32_16x16x32_bf16 v[34:37], v[190:193], v[206:209], v[34:37]
	v_mfma_f32_16x16x32_bf16 v[22:25], v[182:185], v[214:217], v[22:25]
	v_mfma_f32_16x16x32_bf16 v[18:21], v[190:193], v[214:217], v[18:21]
	v_mfma_f32_16x16x32_bf16 v[6:9], v[182:185], v[234:237], v[6:9]
	v_mfma_f32_16x16x32_bf16 v[2:5], v[190:193], v[234:237], v[2:5]
	s_setprio 0

.Lt10_flag:
.LBB0_1479:
	s_add_u32 s38, s22, s34
	s_addc_u32 s39, s23, s35
	s_add_u32 s38, s38, 0x100
	s_addc_u32 s39, s39, 0
	s_add_u32 s55, s50, s34
	s_addc_u32 s56, s51, s35
	s_add_i32 s57, 0, 0x10000
	s_cmpk_eq_i32 s34, 0x300
	s_cselect_b32 s41, s19, s39
	s_cselect_b32 s40, s52, s38
	v_add_u32_e32 v114, s57, v182
	s_cselect_b32 s39, s21, s56
	s_cselect_b32 s38, s53, s55
	s_add_i32 s55, 0, 0x14000
	ds_read_b128 v[136:139], v114
	ds_read_b128 v[152:155], v114 offset:1024
	ds_read_b128 v[156:159], v114 offset:2048
	ds_read_b128 v[160:163], v114 offset:3072
	v_add_u32_e32 v114, s55, v182
	ds_read_b128 v[188:191], v114
	ds_read_b128 v[192:195], v114 offset:1024
	ds_read_b128 v[196:199], v114 offset:2048
	ds_read_b128 v[200:203], v114 offset:3072
	v_lshl_add_u64 v[164:165], v[132:133], 0, s[34:35]
	s_add_i32 m0, s43, 0xc000
	s_bitcmp1_b32 s37, 0
	s_cbranch_scc1 .Lt10_r0
	ds_read_b128 v[204:207], v184
	ds_read_b128 v[208:211], v184 offset:1024
	ds_read_b128 v[212:215], v184 offset:2048
	ds_read_b128 v[216:219], v184 offset:3072
	ds_read_b128 v[220:223], v184 offset:4096
	ds_read_b128 v[234:237], v184 offset:5120
	ds_read_b128 v[238:241], v184 offset:6144
	ds_read_b128 v[242:245], v184 offset:7168
.Lt10_r0:
	global_load_lds_dwordx4 v[164:165], off
	v_lshl_add_u64 v[164:165], v[134:135], 0, s[34:35]
	s_add_i32 m0, s43, 0xe000
	s_nop 0
	global_load_lds_dwordx4 v[164:165], off
	s_waitcnt vmcnt(8)
	s_waitcnt lgkmcnt(0)
	s_barrier
	s_bitcmp1_b32 s37, 0
	s_cbranch_scc1 .Lt10_k0
	s_setprio 1
	s_waitcnt lgkmcnt(0)
	v_mfma_f32_16x16x32_bf16 v[6:9], v[136:139], v[204:207], v[6:9]
	v_mfma_f32_16x16x32_bf16 v[128:131], v[156:159], v[204:207], v[128:131]
	v_mfma_f32_16x16x32_bf16 v[124:127], v[136:139], v[212:215], v[124:127]
	v_mfma_f32_16x16x32_bf16 v[120:123], v[156:159], v[212:215], v[120:123]
	v_mfma_f32_16x16x32_bf16 v[116:119], v[136:139], v[220:223], v[116:119]
	v_mfma_f32_16x16x32_bf16 v[110:113], v[156:159], v[220:223], v[110:113]
	v_mfma_f32_16x16x32_bf16 v[106:109], v[136:139], v[238:241], v[106:109]
	v_mfma_f32_16x16x32_bf16 v[102:105], v[156:159], v[238:241], v[102:105]
	v_mfma_f32_16x16x32_bf16 v[6:9], v[152:155], v[208:211], v[6:9]
	v_mfma_f32_16x16x32_bf16 v[128:131], v[160:163], v[208:211], v[128:131]
	v_mfma_f32_16x16x32_bf16 v[124:127], v[152:155], v[216:219], v[124:127]
	v_mfma_f32_16x16x32_bf16 v[120:123], v[160:163], v[216:219], v[120:123]
	v_mfma_f32_16x16x32_bf16 v[116:119], v[152:155], v[234:237], v[116:119]
	v_mfma_f32_16x16x32_bf16 v[110:113], v[160:163], v[234:237], v[110:113]
	v_mfma_f32_16x16x32_bf16 v[106:109], v[152:155], v[242:245], v[106:109]
	v_mfma_f32_16x16x32_bf16 v[102:105], v[160:163], v[242:245], v[102:105]
	s_setprio 0
	s_setprio 1
	v_mfma_f32_16x16x32_bf16 v[98:101], v[188:191], v[204:207], v[98:101]
	v_mfma_f32_16x16x32_bf16 v[94:97], v[196:199], v[204:207], v[94:97]
	v_mfma_f32_16x16x32_bf16 v[90:93], v[188:191], v[212:215], v[90:93]
	v_mfma_f32_16x16x32_bf16 v[86:89], v[196:199], v[212:215], v[86:89]
	v_mfma_f32_16x16x32_bf16 v[82:85], v[188:191], v[220:223], v[82:85]
	v_mfma_f32_16x16x32_bf16 v[78:81], v[196:199], v[220:223], v[78:81]
	v_mfma_f32_16x16x32_bf16 v[74:77], v[188:191], v[238:241], v[74:77]
	v_mfma_f32_16x16x32_bf16 v[70:73], v[196:199], v[238:241], v[70:73]
	v_mfma_f32_16x16x32_bf16 v[98:101], v[192:195], v[208:211], v[98:101]
	v_mfma_f32_16x16x32_bf16 v[94:97], v[200:203], v[208:211], v[94:97]
	v_mfma_f32_16x16x32_bf16 v[90:93], v[192:195], v[216:219], v[90:93]
	v_mfma_f32_16x16x32_bf16 v[86:89], v[200:203], v[216:219], v[86:89]
	v_mfma_f32_16x16x32_bf16 v[82:85], v[192:195], v[234:237], v[82:85]
	v_mfma_f32_16x16x32_bf16 v[78:81], v[200:203], v[234:237], v[78:81]
	v_mfma_f32_16x16x32_bf16 v[74:77], v[192:195], v[242:245], v[74:77]
	v_mfma_f32_16x16x32_bf16 v[70:73], v[200:203], v[242:245], v[70:73]
	s_setprio 0
.Lt10_k0:
	s_barrier
	s_add_i32 s56, s57, s42
	v_lshl_add_u64 v[164:165], s[38:39], 0, v[142:143]
	s_mov_b32 m0, s56
	s_bitcmp1_b32 s37, 1
	s_cbranch_scc1 .Lt10_r1
	ds_read_b128 v[204:207], v184 offset:16384
	ds_read_b128 v[208:211], v184 offset:17408
	ds_read_b128 v[212:215], v184 offset:18432
	ds_read_b128 v[216:219], v184 offset:19456
	ds_read_b128 v[220:223], v184 offset:20480
	ds_read_b128 v[234:237], v184 offset:21504
	ds_read_b128 v[238:241], v184 offset:22528
	ds_read_b128 v[242:245], v184 offset:23552
.Lt10_r1:
	global_load_lds_dwordx4 v[164:165], off
	s_add_i32 m0, s56, 0x2000
	s_add_u32 s56, s38, 0x20000
	v_lshl_add_u64 v[246:247], s[38:39], 0, v[146:147]
	s_addc_u32 s57, s39, 0
	s_add_i32 s55, s55, s42
	global_load_lds_dwordx4 v[246:247], off
	v_lshl_add_u64 v[248:249], s[56:57], 0, v[142:143]
	s_mov_b32 m0, s55
	v_lshl_add_u64 v[230:231], s[40:41], 0, v[144:145]
	global_load_lds_dwordx4 v[248:249], off
	v_lshl_add_u64 v[248:249], s[56:57], 0, v[146:147]
	s_add_i32 m0, s55, 0x2000
	s_nop 0
	global_load_lds_dwordx4 v[248:249], off
	v_lshl_add_u64 v[248:249], s[40:41], 0, v[140:141]
	s_mov_b32 m0, s43
	s_nop 0
	global_load_lds_dwordx4 v[248:249], off
	s_mov_b32 m0, s44
	s_nop 0
	global_load_lds_dwordx4 v[230:231], off
	s_waitcnt vmcnt(8)
	s_waitcnt lgkmcnt(0)
	s_barrier
	s_bitcmp1_b32 s37, 1
	s_cbranch_scc1 .Lt10_k1
	s_setprio 1
	s_waitcnt lgkmcnt(0)
	v_mfma_f32_16x16x32_bf16 v[66:69], v[136:139], v[204:207], v[66:69]
	v_mfma_f32_16x16x32_bf16 v[62:65], v[156:159], v[204:207], v[62:65]
	v_mfma_f32_16x16x32_bf16 v[58:61], v[136:139], v[212:215], v[58:61]
	v_mfma_f32_16x16x32_bf16 v[54:57], v[156:159], v[212:215], v[54:57]
	v_mfma_f32_16x16x32_bf16 v[50:53], v[136:139], v[220:223], v[50:53]
	v_mfma_f32_16x16x32_bf16 v[46:49], v[156:159], v[220:223], v[46:49]
	v_mfma_f32_16x16x32_bf16 v[42:45], v[136:139], v[238:241], v[42:45]
	v_mfma_f32_16x16x32_bf16 v[38:41], v[156:159], v[238:241], v[38:41]
	v_mfma_f32_16x16x32_bf16 v[66:69], v[152:155], v[208:211], v[66:69]
	v_mfma_f32_16x16x32_bf16 v[62:65], v[160:163], v[208:211], v[62:65]
	v_mfma_f32_16x16x32_bf16 v[58:61], v[152:155], v[216:219], v[58:61]
	v_mfma_f32_16x16x32_bf16 v[54:57], v[160:163], v[216:219], v[54:57]
	v_mfma_f32_16x16x32_bf16 v[50:53], v[152:155], v[234:237], v[50:53]
	v_mfma_f32_16x16x32_bf16 v[46:49], v[160:163], v[234:237], v[46:49]
	v_mfma_f32_16x16x32_bf16 v[42:45], v[152:155], v[242:245], v[42:45]
	v_mfma_f32_16x16x32_bf16 v[38:41], v[160:163], v[242:245], v[38:41]
	s_setprio 0
	s_setprio 1
	v_mfma_f32_16x16x32_bf16 v[34:37], v[188:191], v[204:207], v[34:37]
	v_mfma_f32_16x16x32_bf16 v[30:33], v[196:199], v[204:207], v[30:33]
	v_mfma_f32_16x16x32_bf16 v[26:29], v[188:191], v[212:215], v[26:29]
	v_mfma_f32_16x16x32_bf16 v[22:25], v[196:199], v[212:215], v[22:25]
	v_mfma_f32_16x16x32_bf16 v[18:21], v[188:191], v[220:223], v[18:21]
	v_mfma_f32_16x16x32_bf16 v[14:17], v[196:199], v[220:223], v[14:17]
	v_mfma_f32_16x16x32_bf16 v[10:13], v[188:191], v[238:241], v[10:13]
	v_mfma_f32_16x16x32_bf16 v[2:5], v[196:199], v[238:241], v[2:5]
	v_mfma_f32_16x16x32_bf16 v[34:37], v[192:195], v[208:211], v[34:37]
	v_mfma_f32_16x16x32_bf16 v[30:33], v[200:203], v[208:211], v[30:33]
	v_mfma_f32_16x16x32_bf16 v[26:29], v[192:195], v[216:219], v[26:29]
	v_mfma_f32_16x16x32_bf16 v[22:25], v[200:203], v[216:219], v[22:25]
	v_mfma_f32_16x16x32_bf16 v[18:21], v[192:195], v[234:237], v[18:21]
	v_mfma_f32_16x16x32_bf16 v[14:17], v[200:203], v[234:237], v[14:17]
	v_mfma_f32_16x16x32_bf16 v[10:13], v[192:195], v[242:245], v[10:13]
	v_mfma_f32_16x16x32_bf16 v[2:5], v[200:203], v[242:245], v[2:5]
	s_setprio 0
.Lt10_k1:
	s_barrier
	s_add_i32 s55, 0, 0x18000
	v_add_u32_e32 v114, s55, v182
	s_add_i32 s56, 0, 0x1c000
	ds_read_b128 v[136:139], v114
	ds_read_b128 v[152:155], v114 offset:1024
	ds_read_b128 v[156:159], v114 offset:2048
	ds_read_b128 v[160:163], v114 offset:3072
	v_add_u32_e32 v114, s56, v182
	ds_read_b128 v[188:191], v114
	ds_read_b128 v[192:195], v114 offset:1024
	ds_read_b128 v[196:199], v114 offset:2048
	ds_read_b128 v[200:203], v114 offset:3072
	s_add_u32 s40, s40, 0x20000
	s_addc_u32 s41, s41, 0
	s_mov_b32 m0, s45
	v_lshl_add_u64 v[168:169], s[40:41], 0, v[140:141]
	s_bitcmp1_b32 s37, 0
	s_cbranch_scc1 .Lt10_r2
	ds_read_b128 v[204:207], v184 offset:32768
	ds_read_b128 v[208:211], v184 offset:33792
	ds_read_b128 v[212:215], v184 offset:34816
	ds_read_b128 v[216:219], v184 offset:35840
	ds_read_b128 v[220:223], v184 offset:36864
	ds_read_b128 v[234:237], v184 offset:37888
	ds_read_b128 v[238:241], v184 offset:38912
	ds_read_b128 v[242:245], v184 offset:39936
.Lt10_r2:
	global_load_lds_dwordx4 v[168:169], off
	v_lshl_add_u64 v[168:169], s[40:41], 0, v[144:145]
	s_mov_b32 m0, s46
	s_nop 0
	global_load_lds_dwordx4 v[168:169], off
	s_waitcnt vmcnt(8)
	s_waitcnt lgkmcnt(0)
	s_barrier
	s_bitcmp1_b32 s37, 0
	s_cbranch_scc1 .Lt10_k2
	s_setprio 1
	s_waitcnt lgkmcnt(0)
	v_mfma_f32_16x16x32_bf16 v[6:9], v[136:139], v[204:207], v[6:9]
	v_mfma_f32_16x16x32_bf16 v[128:131], v[156:159], v[204:207], v[128:131]
	v_mfma_f32_16x16x32_bf16 v[124:127], v[136:139], v[212:215], v[124:127]
	v_mfma_f32_16x16x32_bf16 v[120:123], v[156:159], v[212:215], v[120:123]
	v_mfma_f32_16x16x32_bf16 v[116:119], v[136:139], v[220:223], v[116:119]
	v_mfma_f32_16x16x32_bf16 v[110:113], v[156:159], v[220:223], v[110:113]
	v_mfma_f32_16x16x32_bf16 v[106:109], v[136:139], v[238:241], v[106:109]
	v_mfma_f32_16x16x32_bf16 v[102:105], v[156:159], v[238:241], v[102:105]
	v_mfma_f32_16x16x32_bf16 v[6:9], v[152:155], v[208:211], v[6:9]
	v_mfma_f32_16x16x32_bf16 v[128:131], v[160:163], v[208:211], v[128:131]
	v_mfma_f32_16x16x32_bf16 v[124:127], v[152:155], v[216:219], v[124:127]
	v_mfma_f32_16x16x32_bf16 v[120:123], v[160:163], v[216:219], v[120:123]
	v_mfma_f32_16x16x32_bf16 v[116:119], v[152:155], v[234:237], v[116:119]
	v_mfma_f32_16x16x32_bf16 v[110:113], v[160:163], v[234:237], v[110:113]
	v_mfma_f32_16x16x32_bf16 v[106:109], v[152:155], v[242:245], v[106:109]
	v_mfma_f32_16x16x32_bf16 v[102:105], v[160:163], v[242:245], v[102:105]
	s_setprio 0
	s_setprio 1
	v_mfma_f32_16x16x32_bf16 v[98:101], v[188:191], v[204:207], v[98:101]
	v_mfma_f32_16x16x32_bf16 v[94:97], v[196:199], v[204:207], v[94:97]
	v_mfma_f32_16x16x32_bf16 v[90:93], v[188:191], v[212:215], v[90:93]
	v_mfma_f32_16x16x32_bf16 v[86:89], v[196:199], v[212:215], v[86:89]
	v_mfma_f32_16x16x32_bf16 v[82:85], v[188:191], v[220:223], v[82:85]
	v_mfma_f32_16x16x32_bf16 v[78:81], v[196:199], v[220:223], v[78:81]
	v_mfma_f32_16x16x32_bf16 v[74:77], v[188:191], v[238:241], v[74:77]
	v_mfma_f32_16x16x32_bf16 v[70:73], v[196:199], v[238:241], v[70:73]
	v_mfma_f32_16x16x32_bf16 v[98:101], v[192:195], v[208:211], v[98:101]
	v_mfma_f32_16x16x32_bf16 v[94:97], v[200:203], v[208:211], v[94:97]
	v_mfma_f32_16x16x32_bf16 v[90:93], v[192:195], v[216:219], v[90:93]
	v_mfma_f32_16x16x32_bf16 v[86:89], v[200:203], v[216:219], v[86:89]
	v_mfma_f32_16x16x32_bf16 v[82:85], v[192:195], v[234:237], v[82:85]
	v_mfma_f32_16x16x32_bf16 v[78:81], v[200:203], v[234:237], v[78:81]
	v_mfma_f32_16x16x32_bf16 v[74:77], v[192:195], v[242:245], v[74:77]
	v_mfma_f32_16x16x32_bf16 v[70:73], v[200:203], v[242:245], v[70:73]
	s_setprio 0
.Lt10_k2:
	s_barrier
	s_add_i32 s40, s55, s42
	v_lshl_add_u64 v[164:165], v[164:165], 0, s[78:79]
	s_mov_b32 m0, s40
	s_bitcmp1_b32 s37, 1
	s_cbranch_scc1 .Lt10_r3
	ds_read_b128 v[204:207], v184 offset:49152
	ds_read_b128 v[208:211], v184 offset:50176
	ds_read_b128 v[212:215], v184 offset:51200
	ds_read_b128 v[216:219], v184 offset:52224
	ds_read_b128 v[220:223], v184 offset:53248
	ds_read_b128 v[234:237], v184 offset:54272
	ds_read_b128 v[238:241], v184 offset:55296
	ds_read_b128 v[242:245], v184 offset:56320
.Lt10_r3:
	global_load_lds_dwordx4 v[164:165], off
	s_add_i32 m0, s40, 0x2000
	s_add_u32 s38, s38, 0x20080
	v_lshl_add_u64 v[164:165], v[246:247], 0, s[78:79]
	s_addc_u32 s39, s39, 0
	s_add_i32 s40, s56, s42
	global_load_lds_dwordx4 v[164:165], off
	v_lshl_add_u64 v[164:165], s[38:39], 0, v[142:143]
	s_mov_b32 m0, s40
	s_nop 0
	global_load_lds_dwordx4 v[164:165], off
	v_lshl_add_u64 v[164:165], s[38:39], 0, v[146:147]
	s_add_i32 m0, s40, 0x2000
	s_nop 0
	global_load_lds_dwordx4 v[164:165], off
	v_lshl_add_u64 v[164:165], v[248:249], 0, s[78:79]
	s_mov_b32 m0, s47
	s_nop 0
	global_load_lds_dwordx4 v[164:165], off
	v_lshl_add_u64 v[164:165], v[230:231], 0, s[78:79]
	s_mov_b32 m0, s48
	s_nop 0
	global_load_lds_dwordx4 v[164:165], off
	s_waitcnt vmcnt(8)
	s_waitcnt lgkmcnt(0)
	s_barrier
	s_bitcmp1_b32 s37, 1
	s_cbranch_scc1 .Lt10_k3
	s_setprio 1
	s_waitcnt lgkmcnt(0)
	v_mfma_f32_16x16x32_bf16 v[66:69], v[136:139], v[204:207], v[66:69]
	v_mfma_f32_16x16x32_bf16 v[62:65], v[156:159], v[204:207], v[62:65]
	v_mfma_f32_16x16x32_bf16 v[58:61], v[136:139], v[212:215], v[58:61]
	v_mfma_f32_16x16x32_bf16 v[54:57], v[156:159], v[212:215], v[54:57]
	v_mfma_f32_16x16x32_bf16 v[50:53], v[136:139], v[220:223], v[50:53]
	v_mfma_f32_16x16x32_bf16 v[46:49], v[156:159], v[220:223], v[46:49]
	v_mfma_f32_16x16x32_bf16 v[42:45], v[136:139], v[238:241], v[42:45]
	v_mfma_f32_16x16x32_bf16 v[38:41], v[156:159], v[238:241], v[38:41]
	v_mfma_f32_16x16x32_bf16 v[66:69], v[152:155], v[208:211], v[66:69]
	v_mfma_f32_16x16x32_bf16 v[62:65], v[160:163], v[208:211], v[62:65]
	v_mfma_f32_16x16x32_bf16 v[58:61], v[152:155], v[216:219], v[58:61]
	v_mfma_f32_16x16x32_bf16 v[54:57], v[160:163], v[216:219], v[54:57]
	v_mfma_f32_16x16x32_bf16 v[50:53], v[152:155], v[234:237], v[50:53]
	v_mfma_f32_16x16x32_bf16 v[46:49], v[160:163], v[234:237], v[46:49]
	v_mfma_f32_16x16x32_bf16 v[42:45], v[152:155], v[242:245], v[42:45]
	v_mfma_f32_16x16x32_bf16 v[38:41], v[160:163], v[242:245], v[38:41]
	s_setprio 0
	s_setprio 1
	v_mfma_f32_16x16x32_bf16 v[34:37], v[188:191], v[204:207], v[34:37]
	v_mfma_f32_16x16x32_bf16 v[30:33], v[196:199], v[204:207], v[30:33]
	v_mfma_f32_16x16x32_bf16 v[26:29], v[188:191], v[212:215], v[26:29]
	v_mfma_f32_16x16x32_bf16 v[22:25], v[196:199], v[212:215], v[22:25]
	v_mfma_f32_16x16x32_bf16 v[18:21], v[188:191], v[220:223], v[18:21]
	v_mfma_f32_16x16x32_bf16 v[14:17], v[196:199], v[220:223], v[14:17]
	v_mfma_f32_16x16x32_bf16 v[10:13], v[188:191], v[238:241], v[10:13]
	v_mfma_f32_16x16x32_bf16 v[2:5], v[196:199], v[238:241], v[2:5]
	v_mfma_f32_16x16x32_bf16 v[34:37], v[192:195], v[208:211], v[34:37]
	v_mfma_f32_16x16x32_bf16 v[30:33], v[200:203], v[208:211], v[30:33]
	v_mfma_f32_16x16x32_bf16 v[26:29], v[192:195], v[216:219], v[26:29]
	v_mfma_f32_16x16x32_bf16 v[22:25], v[200:203], v[216:219], v[22:25]
	v_mfma_f32_16x16x32_bf16 v[18:21], v[192:195], v[234:237], v[18:21]
	v_mfma_f32_16x16x32_bf16 v[14:17], v[200:203], v[234:237], v[14:17]
	v_mfma_f32_16x16x32_bf16 v[10:13], v[192:195], v[242:245], v[10:13]
	v_mfma_f32_16x16x32_bf16 v[2:5], v[200:203], v[242:245], v[2:5]
	s_setprio 0
